# phase 1 row loop: next row's 8 loads prefetched into a second register set while the current row is normalised; on top of v41
# speedup vs baseline: 1.0154x; 1.0025x over previous
; #define GAS __attribute__((address_space(1)))
; __device__ __forceinline__ float dot4(f32x4 a, f32x4 b) { return (a.x * b.x + a.y * b.y) + (a.z * b.z + a.w * b.w); }
; __device__ __forceinline__ void phase1(KP kp, LAS unsigned char* lds, int wave, int bid, int G) {
;     ...
;     for (int m = bid * NWAVES + wave; m < T; m += G * NWAVES) {
;         const GAS f32x4* xr = (const GAS f32x4*)(x + (size_t)m * DM) + lane;
;         f32x4 v[8]; float s = 0.f;
; #pragma unroll
;         for (int j = 0; j < 8; ++j) { v[j] = xr[64 * j]; s += dot4(v[j], v[j]); }
;         const float rstd = 1.0f / sqrtf(wave_sum(s) * (1.0f / DM) + EPS);
.LBB0_135:
	global_load_dwordx4 v[160:163], v[82:83], off offset:-3072
	global_load_dwordx4 v[164:167], v[82:83], off offset:-2048
	global_load_dwordx4 v[168:171], v[82:83], off
	global_load_dwordx4 v[172:175], v[82:83], off offset:-1024
	v_add_co_u32_e32 v84, vcc, 0xfffff000, v82
	s_nop 1
	v_addc_co_u32_e32 v85, vcc, -1, v83, vcc
	global_load_dwordx4 v[176:179], v[84:85], off offset:-3072
	global_load_dwordx4 v[180:183], v[84:85], off offset:-2048
	global_load_dwordx4 v[184:187], v[84:85], off offset:-1024
	global_load_dwordx4 v[188:191], v[82:83], off offset:-4096
	v_lshl_add_u64 v[82:83], v[82:83], 0, s[12:13]
	s_waitcnt vmcnt(0)
.Lp1row_loop:
	v_mov_b32_e32 v64, v160
	v_mov_b32_e32 v65, v161
	v_mov_b32_e32 v66, v162
	v_mov_b32_e32 v67, v163
	v_mov_b32_e32 v68, v164
	v_mov_b32_e32 v69, v165
	v_mov_b32_e32 v70, v166
	v_mov_b32_e32 v71, v167
	v_mov_b32_e32 v72, v168
	v_mov_b32_e32 v73, v169
	v_mov_b32_e32 v74, v170
	v_mov_b32_e32 v75, v171
	v_mov_b32_e32 v76, v172
	v_mov_b32_e32 v77, v173
	v_mov_b32_e32 v78, v174
	v_mov_b32_e32 v79, v175
	v_mov_b32_e32 v94, v176
	v_mov_b32_e32 v95, v177
	v_mov_b32_e32 v96, v178
	v_mov_b32_e32 v97, v179
	v_mov_b32_e32 v98, v180
	v_mov_b32_e32 v99, v181
	v_mov_b32_e32 v100, v182
	v_mov_b32_e32 v101, v183
	v_mov_b32_e32 v102, v184
	v_mov_b32_e32 v103, v185
	v_mov_b32_e32 v104, v186
	v_mov_b32_e32 v105, v187
	v_mov_b32_e32 v106, v188
	v_mov_b32_e32 v107, v189
	v_mov_b32_e32 v108, v190
	v_mov_b32_e32 v109, v191
	s_add_i32 s8, s8, s10
	s_cmpk_lt_i32 s8, 0x2000
	s_cbranch_scc0 .Lp1row_nopf
	global_load_dwordx4 v[160:163], v[82:83], off offset:-3072
	global_load_dwordx4 v[164:167], v[82:83], off offset:-2048
	global_load_dwordx4 v[168:171], v[82:83], off
	global_load_dwordx4 v[172:175], v[82:83], off offset:-1024
	v_add_co_u32_e32 v84, vcc, 0xfffff000, v82
	s_nop 1
	v_addc_co_u32_e32 v85, vcc, -1, v83, vcc
	global_load_dwordx4 v[176:179], v[84:85], off offset:-3072
	global_load_dwordx4 v[180:183], v[84:85], off offset:-2048
	global_load_dwordx4 v[184:187], v[84:85], off offset:-1024
	global_load_dwordx4 v[188:191], v[82:83], off offset:-4096
	v_lshl_add_u64 v[82:83], v[82:83], 0, s[12:13]
.Lp1row_nopf:
	v_mul_f32_e32 v131, v64, v64
	v_pk_mul_f32 v[84:85], v[70:71], v[70:71]
	v_pk_mul_f32 v[110:111], v[68:69], v[68:69]
	v_mul_f32_e32 v112, v77, v77
	v_mul_f32_e32 v114, v79, v79
	v_mul_f32_e32 v129, v74, v74
	v_mul_f32_e32 v137, v75, v75
	v_pk_mov_b32 v[116:117], v[110:111], v[84:85] op_sel:[1,0]
	v_mov_b32_e32 v111, v85
	v_pk_fma_f32 v[84:85], v[76:77], v[76:77], v[112:113] op_sel_hi:[1,1,0]
	v_pk_fma_f32 v[112:113], v[78:79], v[78:79], v[114:115] op_sel_hi:[1,1,0]
	v_mov_b32_e32 v118, v95
	v_mov_b32_e32 v119, v99
	v_mov_b32_e32 v122, v97
	v_mov_b32_e32 v123, v101
	v_mov_b32_e32 v114, v94
	v_mov_b32_e32 v115, v98
	v_mov_b32_e32 v120, v96
	v_mov_b32_e32 v121, v100
	v_pk_mul_f32 v[124:125], v[104:105], v[104:105]
	v_pk_mul_f32 v[126:127], v[102:103], v[102:103]
	v_pk_add_f32 v[110:111], v[116:117], v[110:111]
	v_mov_b32_e32 v85, v129
	v_mov_b32_e32 v113, v137
	v_pk_mul_f32 v[116:117], v[118:119], v[118:119]
	v_pk_mul_f32 v[118:119], v[122:123], v[122:123]
	v_pk_mov_b32 v[122:123], v[126:127], v[124:125] op_sel:[1,0]
	v_mov_b32_e32 v127, v125
	v_pk_add_f32 v[84:85], v[84:85], v[112:113]
	v_pk_fma_f32 v[112:113], v[114:115], v[114:115], v[116:117]
	v_pk_fma_f32 v[114:115], v[120:121], v[120:121], v[118:119]
	v_mul_f32_e32 v128, v107, v107
	v_mul_f32_e32 v130, v109, v109
	v_pk_add_f32 v[116:117], v[122:123], v[126:127]
	v_pk_add_f32 v[112:113], v[112:113], v[114:115]
	v_mul_f32_e32 v132, v65, v65
	v_mul_f32_e32 v133, v66, v66
	v_mul_f32_e32 v134, v67, v67
	v_pk_fma_f32 v[124:125], v[106:107], v[106:107], v[128:129] op_sel_hi:[1,1,0]
	v_pk_fma_f32 v[128:129], v[108:109], v[108:109], v[130:131] op_sel_hi:[1,1,0]
	v_pk_add_f32 v[114:115], v[116:117], v[116:117] op_sel:[0,1] op_sel_hi:[1,0]
	v_pk_add_f32 v[112:113], v[112:113], v[112:113] op_sel:[0,1] op_sel_hi:[1,0]
	v_mov_b32_e32 v125, v133
	v_mov_b32_e32 v129, v134
	v_mov_b32_e32 v115, v132
	v_mov_b32_e32 v113, v131
	v_pk_add_f32 v[116:117], v[124:125], v[128:129]
	v_pk_add_f32 v[112:113], v[112:113], v[114:115]
	v_mul_f32_e32 v135, v72, v72
	v_pk_add_f32 v[112:113], v[112:113], v[116:117]
	v_mul_f32_e32 v136, v73, v73
	v_pk_add_f32 v[110:111], v[110:111], v[110:111] op_sel:[0,1] op_sel_hi:[1,0]
	v_pk_add_f32 v[112:113], v[112:113], v[112:113] op_sel:[0,1] op_sel_hi:[1,0]
	v_mov_b32_e32 v111, v136
	v_mov_b32_e32 v113, v135
	v_pk_add_f32 v[110:111], v[112:113], v[110:111]
	s_nop 0
	v_pk_add_f32 v[84:85], v[110:111], v[84:85]
	s_nop 0
	v_add_f32_e32 v84, v84, v85
	s_nop 1
	v_add_f32_dpp v84, v84, v84 quad_perm:[1,0,3,2] row_mask:0xf bank_mask:0xf
	s_nop 1
	v_add_f32_dpp v84, v84, v84 quad_perm:[2,3,0,1] row_mask:0xf bank_mask:0xf
	s_nop 1
	v_add_f32_dpp v84, v84, v84 row_half_mirror row_mask:0xf bank_mask:0xf
	s_nop 1
	v_add_f32_dpp v84, v84, v84 row_mirror row_mask:0xf bank_mask:0xf
	v_mov_b32_e32 v85, v84
	s_nop 1
	v_permlane16_swap_b32_e32 v84, v85
	v_add_f32_e32 v84, v84, v85
	v_mov_b32_e32 v85, v84
	s_nop 1
	v_permlane32_swap_b32_e32 v84, v85
	v_add_f32_e32 v84, v84, v85
	v_fmamk_f32 v84, v84, 0x3a000000, v92
	v_mul_f32_e32 v85, 0x4f800000, v84
	v_cmp_gt_f32_e32 vcc, s4, v84
	s_nop 1
	v_cndmask_b32_e32 v84, v84, v85, vcc
	v_sqrt_f32_e32 v85, v84
	s_nop 0
	v_add_u32_e32 v110, -1, v85
	v_add_u32_e32 v111, 1, v85
	v_fma_f32 v112, -v110, v85, v84
	v_fma_f32 v113, -v111, v85, v84
	v_cmp_ge_f32_e64 s[2:3], 0, v112
	s_nop 1
	v_cndmask_b32_e64 v85, v85, v110, s[2:3]
	v_cmp_lt_f32_e64 s[2:3], 0, v113
	s_nop 1
	v_cndmask_b32_e64 v85, v85, v111, s[2:3]
	v_mul_f32_e32 v110, 0x37800000, v85
; #define GAS __attribute__((address_space(1)))
; #define LAS __attribute__((address_space(3)))
; __device__ __forceinline__ u32x2 pack4(f32x4 v) { u32x2 w; w.x = pk2(v.x, v.y); w.y = pk2(v.z, v.w); return w; }
; __device__ __forceinline__ void phase1(KP kp, LAS unsigned char* lds, int wave, int bid, int G) {
;     ...
;         const float rstd = 1.0f / sqrtf(wave_sum(s) * (1.0f / DM) + EPS);
;         GAS u32x2* o8 = (GAS u32x2*)(H + (size_t)m * DM) + lane;
; #pragma unroll
;         for (int j = 0; j < 8; ++j) { const f32x4 av = *(const LAS f32x4*)(A1 + 256 * j + 4 * lane), bv = *(const LAS f32x4*)(B1 + 256 * j + 4 * lane);
;             o8[64 * j] = pack4(v[j] * rstd * av + bv); }
;     }
	v_cndmask_b32_e32 v85, v85, v110, vcc
	v_cmp_class_f32_e32 vcc, v84, v93
	s_nop 1
	v_cndmask_b32_e32 v84, v85, v84, vcc
	v_div_scale_f32 v85, s[2:3], v84, v84, 1.0
	v_rcp_f32_e32 v111, v85
	v_div_scale_f32 v110, vcc, 1.0, v84, 1.0
	v_fma_f32 v112, -v85, v111, 1.0
	v_fmac_f32_e32 v111, v112, v111
	v_mul_f32_e32 v112, v110, v111
	v_fma_f32 v113, -v85, v112, v110
	v_fmac_f32_e32 v112, v113, v111
	v_fma_f32 v85, -v85, v112, v110
	v_div_fmas_f32 v85, v85, v111, v112
	v_div_fixup_f32 v84, v85, v84, 1.0
	v_pk_mul_f32 v[94:95], v[94:95], v[84:85] op_sel_hi:[1,0]
	v_pk_mul_f32 v[96:97], v[96:97], v[84:85] op_sel_hi:[1,0]
	v_pk_mul_f32 v[98:99], v[98:99], v[84:85] op_sel_hi:[1,0]
	v_pk_mul_f32 v[100:101], v[100:101], v[84:85] op_sel_hi:[1,0]
	v_pk_mul_f32 v[102:103], v[102:103], v[84:85] op_sel_hi:[1,0]
	v_pk_mul_f32 v[104:105], v[104:105], v[84:85] op_sel_hi:[1,0]
	v_pk_mul_f32 v[106:107], v[106:107], v[84:85] op_sel_hi:[1,0]
	v_pk_mul_f32 v[108:109], v[108:109], v[84:85] op_sel_hi:[1,0]
	v_pk_mul_f32 v[64:65], v[64:65], v[84:85] op_sel_hi:[1,0]
	v_pk_mul_f32 v[66:67], v[66:67], v[84:85] op_sel_hi:[1,0]
	v_pk_mul_f32 v[68:69], v[68:69], v[84:85] op_sel_hi:[1,0]
	v_pk_mul_f32 v[70:71], v[70:71], v[84:85] op_sel_hi:[1,0]
	v_pk_mul_f32 v[76:77], v[76:77], v[84:85] op_sel_hi:[1,0]
	v_pk_mul_f32 v[78:79], v[78:79], v[84:85] op_sel_hi:[1,0]
	v_pk_mul_f32 v[72:73], v[72:73], v[84:85] op_sel_hi:[1,0]
	v_pk_mul_f32 v[74:75], v[74:75], v[84:85] op_sel_hi:[1,0]
	v_pk_fma_f32 v[84:85], v[2:3], v[96:97], v[10:11]
	v_pk_fma_f32 v[94:95], v[0:1], v[94:95], v[8:9]
	v_pk_fma_f32 v[96:97], v[6:7], v[100:101], v[14:15]
	v_pk_fma_f32 v[98:99], v[4:5], v[98:99], v[12:13]
	v_pk_fma_f32 v[100:101], v[18:19], v[104:105], v[26:27]
	v_pk_fma_f32 v[102:103], v[16:17], v[102:103], v[24:25]
	v_pk_fma_f32 v[104:105], v[22:23], v[108:109], v[30:31]
	v_pk_fma_f32 v[106:107], v[20:21], v[106:107], v[28:29]
	v_pk_fma_f32 v[66:67], v[34:35], v[66:67], v[42:43]
	v_pk_fma_f32 v[64:65], v[32:33], v[64:65], v[40:41]
	v_pk_fma_f32 v[70:71], v[38:39], v[70:71], v[46:47]
	v_pk_fma_f32 v[68:69], v[36:37], v[68:69], v[44:45]
	v_pk_fma_f32 v[78:79], v[50:51], v[78:79], v[58:59]
	v_pk_fma_f32 v[76:77], v[48:49], v[76:77], v[56:57]
	v_pk_fma_f32 v[74:75], v[54:55], v[74:75], v[62:63]
	v_pk_fma_f32 v[72:73], v[52:53], v[72:73], v[60:61]
	v_bfe_u32 v108, v94, 16, 1
	v_bfe_u32 v110, v84, 16, 1
	v_bfe_u32 v109, v95, 16, 1
	v_bfe_u32 v111, v85, 16, 1
	v_bfe_u32 v112, v98, 16, 1
	v_bfe_u32 v114, v96, 16, 1
	v_bfe_u32 v116, v102, 16, 1
	v_bfe_u32 v118, v100, 16, 1
	v_bfe_u32 v120, v106, 16, 1
	v_bfe_u32 v122, v104, 16, 1
	v_bfe_u32 v124, v64, 16, 1
	v_bfe_u32 v125, v65, 16, 1
	v_bfe_u32 v126, v66, 16, 1
	v_bfe_u32 v127, v67, 16, 1
	v_bfe_u32 v128, v68, 16, 1
	v_bfe_u32 v129, v69, 16, 1
	v_bfe_u32 v130, v70, 16, 1
	v_bfe_u32 v131, v71, 16, 1
	v_bfe_u32 v132, v76, 16, 1
	v_bfe_u32 v134, v78, 16, 1
	v_bfe_u32 v136, v72, 16, 1
	v_bfe_u32 v137, v73, 16, 1
	v_bfe_u32 v138, v74, 16, 1
	v_add3_u32 v94, v94, v108, s5
	v_add3_u32 v84, v84, v110, s5
	v_bfe_u32 v113, v99, 16, 1
	v_bfe_u32 v115, v97, 16, 1
	v_bfe_u32 v117, v103, 16, 1
	v_bfe_u32 v119, v101, 16, 1
	v_bfe_u32 v121, v107, 16, 1
	v_bfe_u32 v123, v105, 16, 1
	v_bfe_u32 v133, v77, 16, 1
	v_bfe_u32 v135, v79, 16, 1
	v_bfe_u32 v139, v75, 16, 1
	v_add3_u32 v95, v95, v109, s5
	v_add3_u32 v85, v85, v111, s5
	v_add3_u32 v98, v98, v112, s5
	v_add3_u32 v96, v96, v114, s5
	v_add3_u32 v102, v102, v116, s5
	v_add3_u32 v100, v100, v118, s5
	v_add3_u32 v106, v106, v120, s5
	v_add3_u32 v104, v104, v122, s5
	v_add3_u32 v64, v64, v124, s5
	v_add3_u32 v108, v65, v125, s5
	v_add3_u32 v65, v66, v126, s5
	v_add3_u32 v109, v67, v127, s5
	v_add3_u32 v66, v68, v128, s5
	v_add3_u32 v110, v69, v129, s5
	v_add3_u32 v67, v70, v130, s5
	v_add3_u32 v111, v71, v131, s5
	v_add3_u32 v68, v76, v132, s5
	v_add3_u32 v69, v78, v134, s5
	v_add3_u32 v70, v72, v136, s5
	v_add3_u32 v78, v73, v137, s5
	v_add3_u32 v71, v74, v138, s5
	v_lshrrev_b32_e32 v72, 16, v94
	v_lshrrev_b32_e32 v73, 16, v84
	v_add3_u32 v99, v99, v113, s5
	v_add3_u32 v97, v97, v115, s5
	v_add3_u32 v103, v103, v117, s5
	v_add3_u32 v101, v101, v119, s5
	v_add3_u32 v107, v107, v121, s5
	v_add3_u32 v105, v105, v123, s5
	v_add3_u32 v76, v77, v133, s5
	v_add3_u32 v77, v79, v135, s5
	v_add3_u32 v79, v75, v139, s5
	v_lshrrev_b32_e32 v74, 16, v98
	v_lshrrev_b32_e32 v75, 16, v96
	v_lshrrev_b32_e32 v84, 16, v102
	v_lshrrev_b32_e32 v94, 16, v100
	v_lshrrev_b32_e32 v96, 16, v106
	v_lshrrev_b32_e32 v98, 16, v104
	v_lshrrev_b32_e32 v100, 16, v64
	v_lshrrev_b32_e32 v102, 16, v65
	v_lshrrev_b32_e32 v104, 16, v66
	v_lshrrev_b32_e32 v106, 16, v67
	v_lshrrev_b32_e32 v112, 16, v68
	v_lshrrev_b32_e32 v113, 16, v69
	v_lshrrev_b32_e32 v114, 16, v70
	v_lshrrev_b32_e32 v115, 16, v71
	v_and_or_b32 v64, v95, s9, v72
	v_and_or_b32 v65, v85, s9, v73
	v_and_or_b32 v66, v99, s9, v74
	v_and_or_b32 v67, v97, s9, v75
	v_and_or_b32 v68, v103, s9, v84
	v_and_or_b32 v69, v101, s9, v94
	v_and_or_b32 v70, v107, s9, v96
	v_and_or_b32 v71, v105, s9, v98
	v_and_or_b32 v72, v108, s9, v100
	v_and_or_b32 v73, v109, s9, v102
	v_and_or_b32 v74, v110, s9, v104
	v_and_or_b32 v75, v111, s9, v106
	v_and_or_b32 v76, v76, s9, v112
	v_and_or_b32 v77, v77, s9, v113
	v_and_or_b32 v78, v78, s9, v114
	v_and_or_b32 v79, v79, s9, v115
	global_store_dwordx2 v[80:81], v[64:65], off offset:-3584
	global_store_dwordx2 v[80:81], v[66:67], off offset:-3072
	global_store_dwordx2 v[80:81], v[68:69], off offset:-2560
	global_store_dwordx2 v[80:81], v[70:71], off offset:-2048
	global_store_dwordx2 v[80:81], v[72:73], off offset:-1536
	global_store_dwordx2 v[80:81], v[74:75], off offset:-1024
	global_store_dwordx2 v[80:81], v[76:77], off offset:-512
	global_store_dwordx2 v[80:81], v[78:79], off
	v_lshl_add_u64 v[80:81], v[80:81], 0, s[6:7]
	s_cmpk_lt_i32 s8, 0x2000
	s_waitcnt vmcnt(8)
	s_cbranch_scc1 .Lp1row_loop
